# baseline (speedup 1.0000x reference)
.Lk2_l1_done:
	v_lshrrev_b32_e32 v29, 5, v1
	v_and_b32_e32 v31, 31, v1
	v_lshl_add_u32 v29, s25, 3, v29
	v_lshlrev_b32_e32 v29, 3, v29
	v_lshlrev_b32_e32 v31, 3, v31
	ds_read_b64 v[116:117], v29 offset:0
	v_mov_b32_e32 v118, 0
	v_mov_b32_e32 v119, 0
	ds_read_b64 v[108:109], v31 offset:0
	ds_read_b64 v[110:111], v31 offset:256
	ds_read_b64 v[112:113], v31 offset:512
	ds_read_b64 v[114:115], v31 offset:768
	s_waitcnt lgkmcnt(0)
	v_add_f64 v[120:121], v[108:109], -v[116:117]
	v_cmp_lt_f64_e32 vcc, s[32:33], v[120:121]
	v_cmp_ge_f64_e64 s[48:49], s[32:33], |v[120:121]|
	s_nop 0
	v_addc_co_u32_e32 v118, vcc, 0, v118, vcc
	v_addc_co_u32_e64 v119, s[50:51], 0, v119, s[48:49]
	v_add_f64 v[120:121], v[110:111], -v[116:117]
	v_cmp_lt_f64_e32 vcc, s[32:33], v[120:121]
	v_cmp_ge_f64_e64 s[48:49], s[32:33], |v[120:121]|
	s_nop 0
	v_addc_co_u32_e32 v118, vcc, 0, v118, vcc
	v_addc_co_u32_e64 v119, s[50:51], 0, v119, s[48:49]
	v_add_f64 v[120:121], v[112:113], -v[116:117]
	v_cmp_lt_f64_e32 vcc, s[32:33], v[120:121]
	v_cmp_ge_f64_e64 s[48:49], s[32:33], |v[120:121]|
	s_nop 0
	v_addc_co_u32_e32 v118, vcc, 0, v118, vcc
	v_addc_co_u32_e64 v119, s[50:51], 0, v119, s[48:49]
	v_add_f64 v[120:121], v[114:115], -v[116:117]
	v_cmp_lt_f64_e32 vcc, s[32:33], v[120:121]
	v_cmp_ge_f64_e64 s[48:49], s[32:33], |v[120:121]|
	s_nop 0
	v_addc_co_u32_e32 v118, vcc, 0, v118, vcc
	v_addc_co_u32_e64 v119, s[50:51], 0, v119, s[48:49]
	ds_read_b64 v[108:109], v31 offset:1024
	ds_read_b64 v[110:111], v31 offset:1280
	ds_read_b64 v[112:113], v31 offset:1536
	ds_read_b64 v[114:115], v31 offset:1792
	s_waitcnt lgkmcnt(0)
	v_add_f64 v[120:121], v[108:109], -v[116:117]
	v_cmp_lt_f64_e32 vcc, s[32:33], v[120:121]
	v_cmp_ge_f64_e64 s[48:49], s[32:33], |v[120:121]|
	s_nop 0
	v_addc_co_u32_e32 v118, vcc, 0, v118, vcc
	v_addc_co_u32_e64 v119, s[50:51], 0, v119, s[48:49]
	v_add_f64 v[120:121], v[110:111], -v[116:117]
	v_cmp_lt_f64_e32 vcc, s[32:33], v[120:121]
	v_cmp_ge_f64_e64 s[48:49], s[32:33], |v[120:121]|
	s_nop 0
	v_addc_co_u32_e32 v118, vcc, 0, v118, vcc
	v_addc_co_u32_e64 v119, s[50:51], 0, v119, s[48:49]
	v_add_f64 v[120:121], v[112:113], -v[116:117]
	v_cmp_lt_f64_e32 vcc, s[32:33], v[120:121]
	v_cmp_ge_f64_e64 s[48:49], s[32:33], |v[120:121]|
	s_nop 0
	v_addc_co_u32_e32 v118, vcc, 0, v118, vcc
	v_addc_co_u32_e64 v119, s[50:51], 0, v119, s[48:49]
	v_add_f64 v[120:121], v[114:115], -v[116:117]
	v_cmp_lt_f64_e32 vcc, s[32:33], v[120:121]
	v_cmp_ge_f64_e64 s[48:49], s[32:33], |v[120:121]|
	s_nop 0
	v_addc_co_u32_e32 v118, vcc, 0, v118, vcc
	v_addc_co_u32_e64 v119, s[50:51], 0, v119, s[48:49]
	ds_read_b64 v[108:109], v31 offset:2048
	ds_read_b64 v[110:111], v31 offset:2304
	ds_read_b64 v[112:113], v31 offset:2560
	ds_read_b64 v[114:115], v31 offset:2816
	s_waitcnt lgkmcnt(0)
	v_add_f64 v[120:121], v[108:109], -v[116:117]
	v_cmp_lt_f64_e32 vcc, s[32:33], v[120:121]
	v_cmp_ge_f64_e64 s[48:49], s[32:33], |v[120:121]|
	s_nop 0
	v_addc_co_u32_e32 v118, vcc, 0, v118, vcc
	v_addc_co_u32_e64 v119, s[50:51], 0, v119, s[48:49]
	v_add_f64 v[120:121], v[110:111], -v[116:117]
	v_cmp_lt_f64_e32 vcc, s[32:33], v[120:121]
	v_cmp_ge_f64_e64 s[48:49], s[32:33], |v[120:121]|
	s_nop 0
	v_addc_co_u32_e32 v118, vcc, 0, v118, vcc
	v_addc_co_u32_e64 v119, s[50:51], 0, v119, s[48:49]
	v_add_f64 v[120:121], v[112:113], -v[116:117]
	v_cmp_lt_f64_e32 vcc, s[32:33], v[120:121]
	v_cmp_ge_f64_e64 s[48:49], s[32:33], |v[120:121]|
	s_nop 0
	v_addc_co_u32_e32 v118, vcc, 0, v118, vcc
	v_addc_co_u32_e64 v119, s[50:51], 0, v119, s[48:49]
	v_add_f64 v[120:121], v[114:115], -v[116:117]
	v_cmp_lt_f64_e32 vcc, s[32:33], v[120:121]
	v_cmp_ge_f64_e64 s[48:49], s[32:33], |v[120:121]|
	s_nop 0
	v_addc_co_u32_e32 v118, vcc, 0, v118, vcc
	v_addc_co_u32_e64 v119, s[50:51], 0, v119, s[48:49]
	ds_read_b64 v[108:109], v31 offset:3072
	ds_read_b64 v[110:111], v31 offset:3328
	ds_read_b64 v[112:113], v31 offset:3584
	ds_read_b64 v[114:115], v31 offset:3840
	s_waitcnt lgkmcnt(0)
	v_add_f64 v[120:121], v[108:109], -v[116:117]
	v_cmp_lt_f64_e32 vcc, s[32:33], v[120:121]
	v_cmp_ge_f64_e64 s[48:49], s[32:33], |v[120:121]|
	s_nop 0
	v_addc_co_u32_e32 v118, vcc, 0, v118, vcc
	v_addc_co_u32_e64 v119, s[50:51], 0, v119, s[48:49]
	v_add_f64 v[120:121], v[110:111], -v[116:117]
	v_cmp_lt_f64_e32 vcc, s[32:33], v[120:121]
	v_cmp_ge_f64_e64 s[48:49], s[32:33], |v[120:121]|
	s_nop 0
	v_addc_co_u32_e32 v118, vcc, 0, v118, vcc
	v_addc_co_u32_e64 v119, s[50:51], 0, v119, s[48:49]
	v_add_f64 v[120:121], v[112:113], -v[116:117]
	v_cmp_lt_f64_e32 vcc, s[32:33], v[120:121]
	v_cmp_ge_f64_e64 s[48:49], s[32:33], |v[120:121]|
	s_nop 0
	v_addc_co_u32_e32 v118, vcc, 0, v118, vcc
	v_addc_co_u32_e64 v119, s[50:51], 0, v119, s[48:49]
	v_add_f64 v[120:121], v[114:115], -v[116:117]
	v_cmp_lt_f64_e32 vcc, s[32:33], v[120:121]
	v_cmp_ge_f64_e64 s[48:49], s[32:33], |v[120:121]|
	s_nop 0
	v_addc_co_u32_e32 v118, vcc, 0, v118, vcc
	v_addc_co_u32_e64 v119, s[50:51], 0, v119, s[48:49]
	v_lshl_or_b32 v122, v119, 16, v118
	s_nop 1
	v_add_u32_dpp v122, v122, v122 quad_perm:[1,0,3,2] row_mask:0xf bank_mask:0xf
	s_nop 1
	v_add_u32_dpp v122, v122, v122 quad_perm:[2,3,0,1] row_mask:0xf bank_mask:0xf
	s_nop 1
	v_add_u32_dpp v122, v122, v122 row_half_mirror row_mask:0xf bank_mask:0xf
	s_nop 1
	v_add_u32_dpp v122, v122, v122 row_mirror row_mask:0xf bank_mask:0xf
	s_nop 1
	v_add_u32_dpp v122, v122, v122 row_bcast:15 row_mask:0xa bank_mask:0xf
	s_nop 1
	v_readlane_b32 s98, v122, 31
	v_readlane_b32 s99, v122, 63
	s_mov_b32 s52, s98
	s_mov_b32 s53, s99
	v_and_b32_e32 v69, 63, v1
	v_lshlrev_b32_e32 v69, 4, v69
	v_add_u32_e32 v70, 0x1000, v69
	s_and_b32 s54, s52, 0xffff
	s_lshr_b32 s55, s52, 16
	s_and_b32 s56, s53, 0xffff
	s_lshr_b32 s57, s53, 16
	s_cmp_gt_u32 s55, 1
	s_cselect_b32 s58, 1, 0
	s_cmp_lt_u32 s54, 0x64
	s_cselect_b32 s59, 1, 0
	s_and_b32 s58, s58, s59
	s_cmp_gt_u32 s57, 1
	s_cselect_b32 s60, 1, 0
	s_cmp_lt_u32 s56, 0x64
	s_cselect_b32 s61, 1, 0
	s_and_b32 s60, s60, s61
	s_or_b32 s61, s58, s60
	s_lshl_b32 s62, s25, 3
	s_lshl_b32 s63, s27, 1
	s_add_u32 s62, s62, s63
	s_add_u32 s62, s62, s26
	s_lshl_b32 s62, s62, 13
	s_add_u32 s64, s6, s62
	s_addc_u32 s65, s7, 0
	s_add_u32 s66, s64, 0x2000
	s_addc_u32 s67, s65, 0
	s_waitcnt vmcnt(0) lgkmcnt(0)
	v_cmp_lt_u32_e32 vcc, 0, v28
	s_cbranch_vccz .Lk2_l2_done
	v_cmp_lt_u32_e32 vcc, 0, v26
	s_and_saveexec_b64 s[46:47], vcc
	s_cbranch_execz .Lk2_l2_0_0
	v_cvt_f64_f32_e32 v[88:89], v32
	v_add_f64 v[88:89], v[88:89], -v[34:35]
	v_add_f64 v[88:89], v[88:89], -v[92:93]
	v_cmp_le_f64_e32 vcc, s[34:35], v[88:89]
	v_cmp_ge_f64_e64 s[48:49], s[32:33], v[88:89]
	s_or_b64 s[36:37], s[36:37], vcc
	s_and_b64 s[48:49], s[48:49], vcc
	s_or_b64 s[44:45], s[44:45], s[48:49]

.Lk2_l2_done:
	s_or_b64 s[94:95], s[36:37], s[40:41]
	s_mov_b64 s[84:85], 0
	s_mov_b64 s[50:51], s[36:37]

.Lk2_t15_c2ok0:
	v_cvt_f64_f32_e32 v[54:55], v47
	v_cvt_f64_f32_e32 v[56:57], v62
	v_add_f64 v[54:55], v[54:55], -v[44:45]
	v_add_f64 v[56:57], v[56:57], -v[50:51]
	v_add_f64 v[58:59], v[54:55], -v[60:61]
	v_add_f64 v[56:57], v[56:57], -v[54:55]
	v_cmp_lt_f64_e64 s[66:67], s[32:33], v[58:59]
	v_cmp_le_f64_e64 s[68:69], s[34:35], v[56:57]
	s_and_b64 s[66:67], s[66:67], s[62:63]
	s_and_b32 s66, s66, 0xff
	s_and_b64 s[68:69], s[68:69], s[64:65]
	s_or_b32 s68, s68, s69
	s_lshr_b32 s69, s68, 16
	s_or_b32 s68, s68, s69
	s_lshr_b32 s69, s68, 8
	s_or_b32 s68, s68, s69
	s_andn2_b32 s66, s66, s68
	s_and_b32 s66, s66, 0xff
	s_cmp_eq_u32 s66, 0
	s_cbranch_scc1 .Lk2_t15_loop0
	s_bitset1_b64 s[84:85], s56
	s_bitset0_b64 s[36:37], s56
	s_branch .Lk2_t15_loop0
.Lk2_t15_done0:
	s_mov_b64 s[86:87], 0
	s_mov_b64 s[50:51], s[40:41]

.Lk2_t15_c2ok1:
	v_cvt_f64_f32_e32 v[54:55], v47
	v_cvt_f64_f32_e32 v[56:57], v62
	v_add_f64 v[54:55], v[54:55], -v[44:45]
	v_add_f64 v[56:57], v[56:57], -v[50:51]
	v_add_f64 v[58:59], v[54:55], -v[60:61]
	v_add_f64 v[56:57], v[56:57], -v[54:55]
	v_cmp_lt_f64_e64 s[66:67], s[32:33], v[58:59]
	v_cmp_le_f64_e64 s[68:69], s[34:35], v[56:57]
	s_and_b64 s[66:67], s[66:67], s[62:63]
	s_and_b32 s66, s66, 0xff
	s_and_b64 s[68:69], s[68:69], s[64:65]
	s_or_b32 s68, s68, s69
	s_lshr_b32 s69, s68, 16
	s_or_b32 s68, s68, s69
	s_lshr_b32 s69, s68, 8
	s_or_b32 s68, s68, s69
	s_andn2_b32 s66, s66, s68
	s_and_b32 s66, s66, 0xff
	s_cmp_eq_u32 s66, 0
	s_cbranch_scc1 .Lk2_t15_loop1
	s_bitset1_b64 s[86:87], s56
	s_bitset0_b64 s[40:41], s56
	s_branch .Lk2_t15_loop1
.Lk2_t15_done1:
	s_or_b64 s[48:49], s[84:85], s[86:87]
	s_cmp_eq_u64 s[48:49], 0
	s_cbranch_scc1 .Lk2_nochg
	s_mov_b64 exec, s[84:85]
	ds_write_b64 v2, v[96:97] offset:0
	ds_write_b32 v104, v14 offset:4096
	s_mov_b64 exec, s[86:87]
	ds_write_b64 v2, v[98:99] offset:8
	ds_write_b32 v104, v15 offset:4100
	s_mov_b64 exec, -1
	v_mov_b32_e32 v30, 1
	ds_write_b32 v105, v30 offset:24

.Lk2_nohard:
	s_mov_b32 s92, 0
	s_cmp_eq_u64 s[94:95], 0
	s_cbranch_scc1 .Lk2_early
	s_mov_b32 s52, s98
	s_mov_b32 s53, s99
	s_and_b32 s54, s52, 0xffff
	s_lshr_b32 s55, s52, 16
	s_and_b32 s56, s53, 0xffff
	s_lshr_b32 s57, s53, 16
	s_cmp_gt_u32 s55, 1
	s_cselect_b32 s58, 1, 0
	s_cmp_lt_u32 s54, 0x64
	s_cselect_b32 s59, 1, 0
	s_and_b32 s58, s58, s59
	s_cmp_gt_u32 s57, 1
	s_cselect_b32 s60, 1, 0
	s_cmp_lt_u32 s56, 0x64
	s_cselect_b32 s61, 1, 0
	s_and_b32 s60, s60, s61
	s_or_b32 s61, s58, s60
	s_lshl_b32 s62, s25, 3
	s_lshl_b32 s63, s27, 1
	s_add_u32 s62, s62, s63
	s_add_u32 s62, s62, s26
	s_lshl_b32 s62, s62, 13
	s_add_u32 s64, s6, s62
	s_addc_u32 s65, s7, 0
	s_add_u32 s66, s64, 0x2000
	s_addc_u32 s67, s65, 0
	s_branch .Lk2_noearly
.Lk2_early:
	s_cmp_lt_u32 s54, 0x64
	s_cbranch_scc0 .Lk2_ea_skip
	global_load_dwordx4 v[32:35], v69, s[64:65] offset:0 nt
	global_load_dwordx4 v[36:39], v69, s[64:65] offset:1024 nt
	global_load_dwordx4 v[40:43], v69, s[64:65] offset:2048 nt
	global_load_dwordx4 v[44:47], v69, s[64:65] offset:3072 nt
	global_load_dwordx4 v[48:51], v70, s[64:65] offset:0 nt
	global_load_dwordx4 v[52:55], v70, s[64:65] offset:1024 nt
	global_load_dwordx4 v[56:59], v70, s[64:65] offset:2048 nt
	global_load_dwordx4 v[60:63], v70, s[64:65] offset:3072 nt
	s_or_b32 s92, s92, 1
